# v55 + static priority raise (7.4) for the younger half (waves 4-7) during the mixer phase (attention + gating units), reset at the following seam
# baseline (speedup 1.0000x reference)
; #define TSTART() do { tph0 = rt(); } while (0)
; #define TSTART() do {} while (0)
; #define WSL() GAS unsigned char* wlg = (GAS unsigned char*)ws; asm volatile("" : "+s"(wlg)); unsigned char* wl = (unsigned char*)wlg; int cb = (int)blockIdx.x, vcu_ = F.vcu, wave_ = F.wave; asm volatile("" : "+s"(cb), "+s"(vcu_), "+s"(wave_))
; #define ATT(i) do { if (S.next(i, au)) attn_body::attn_unit<8>(au.bh / attn_body::NHEAD, au.bh % attn_body::NHEAD, au.qb, AT.Q, AT.K, AT.V, AT.O, AT.kbarp, (char*)lds + RING_OFF, (unsigned*)(wl + WS_CTL) + 3000); } while (0)
; __global__ void __launch_bounds__(NWAVES * 64, 2) mk_fwd(Args args) {
;     ...
;         if (IN(pb + 1)) { TSTART();
;             WSL(); const bf16* WL = (const bf16*)(wl + WS_W) + (size_t)l * LAYER_W_ELEMS;
;             const attn_body::AttnTensors AT{(const attn_body::bf16*)(wl + WS_Q), (const attn_body::bf16*)(wl + WS_K), (const attn_body::bf16*)(wl + WS_VA), (attn_body::bf16*)(wl + WS_YB), (const float*)(wl + WS_KBARP)};
;             const attn_body::PairOrder S(vcu_); attn_body::AttnUnit au;
;             const bool sgu_first = ((vcu_ >> 1) & 1) == 0;
;     ...
; #pragma unroll 1
;             for (int slot = 0; slot < 3; ++slot) {
;     ...
;                 const int spos = (vcu_ >> 1) % 3;
;                 const int what = slot == spos ? -1 : (slot < spos ? slot : slot - 1);
;     ...
;                 const int what = sgu_first ? slot - 1 : (slot == 1 ? -1 : (slot >> 1));
;     ...
;                 if (what < 0) SGU(); else ATT(what);
.LBB0_804:
	v_readfirstlane_b32 s4, v0
	s_nop 3
	s_bfe_u32 s4, s4, 0x40006
	s_cmp_ge_u32 s4, 4
	s_cbranch_scc0 .Lap_skip
	s_setprio 1
